# baseline (speedup 1.0000x reference)
_Z16sum_layer_kernelPKfS0_Pf:
	s_load_dwordx4 s[4:7], s[0:1], 0x0
	s_load_dwordx2 s[8:9], s[0:1], 0x10
	v_lshrrev_b32_e32 v42, 6, v0
	v_bfe_u32 v41, v0, 5, 1
	v_and_b32_e32 v40, 31, v0
	v_readfirstlane_b32 s23, v42
	v_and_b32_e32 v43, 7, v0
	v_bfe_u32 v44, v0, 3, 3
	s_lshl_b32 s3, s2, 12
	s_lshl_b32 s19, s2, 7
	s_lshl_b32 s23, s23, 12
	v_lshlrev_b32_e32 v1, 11, v41
	v_lshl_or_b32 v1, v40, 2, v1
	s_mov_b32 m0, s23
	v_lshrrev_b32_e32 v46, 1, v44
	v_xor_b32_e32 v46, v43, v46
	v_lshlrev_b32_e32 v46, 4, v46
	v_lshl_add_u32 v35, v44, 16, v46
	v_lshl_add_u32 v35, v42, 21, v35
	v_add_u32_e32 v35, s19, v35
	v_xor_b32_e32 v86, 64, v35
	s_mov_b32 s20, 0x7fc00
	s_mov_b32 s21, 0xff800
	s_mov_b32 s22, 0x17f400
	s_mov_b32 s14, 0x200000
	s_mov_b32 s15, 0x20000
	v_and_b32_e32 v45, 63, v0
	v_lshlrev_b32_e32 v37, 4, v45
	s_lshr_b32 s54, s23, 2
	s_add_u32 s55, s3, s54
	s_add_u32 s54, s54, 0x4000
	s_waitcnt lgkmcnt(0)
	s_mov_b32 s12, s6
	s_and_b32 s13, s7, 0xffff
	s_and_b32 s5, s5, 0xffff
	s_mov_b32 s6, 0x800000
	s_mov_b32 s7, s15
	s_mov_b32 m0, s54
	s_nop 0
	buffer_load_dwordx4 v37, s[12:15], s55 offen nt lds
	s_mov_b32 m0, s23
	s_nop 0
	buffer_load_dwordx4 v35, s[4:7], 0 offen nt lds
	buffer_load_dwordx4 v86, s[4:7], s20 offen offset:1024 nt lds
	buffer_load_dwordx4 v35, s[4:7], s21 offen offset:2048 nt lds
	buffer_load_dwordx4 v86, s[4:7], s22 offen offset:3072 nt lds
	v_and_b32_e32 v45, 63, v0
	v_lshlrev_b32_e32 v36, 2, v40
	v_lshl_add_u32 v36, v41, 18, v36
	v_lshl_add_u32 v36, v42, 21, v36
	v_add_u32_e32 v36, s19, v36
	v_bfe_u32 v47, v40, 1, 3
	v_lshlrev_b32_e32 v39, 2, v41
	v_xor_b32_e32 v39, v39, v47
	v_lshlrev_b32_e32 v39, 4, v39
	v_lshl_add_u32 v39, v40, 7, v39
	v_lshl_add_u32 v39, v42, 12, v39
	v_xor_b32_e32 v81, 16, v39
	v_xor_b32_e32 v82, 32, v39
	v_xor_b32_e32 v83, 48, v39
	v_cmp_gt_u32_e32 vcc, 32, v45
	v_mov_b32_e32 v34, 0xc1600000
	v_mov_b32_e32 v84, 0x3fb8aa3b
	v_mov_b32_e32 v85, 0x3f317218
	s_lshl_b32 s24, 1, 16
	s_lshl_b32 s25, 2, 16
	s_lshl_b32 s26, 3, 16
	s_lshl_b32 s27, 8, 16
	s_lshl_b32 s28, 9, 16
	s_lshl_b32 s29, 10, 16
	s_lshl_b32 s30, 11, 16
	s_lshl_b32 s31, 16, 16
	s_lshl_b32 s32, 17, 16
	s_lshl_b32 s33, 18, 16
	s_lshl_b32 s34, 19, 16
	s_lshl_b32 s35, 24, 16
	s_lshl_b32 s36, 25, 16
	s_lshl_b32 s37, 26, 16
	s_lshl_b32 s38, 27, 16
	s_and_b32 s9, s9, 0xffff
	s_mov_b32 s10, s6
	s_mov_b32 s11, s15
	v_add_u32_e32 v38, 0x4000, v1
	v_add_u32_e32 v87, 0x400, v38
	s_waitcnt vmcnt(4)
	s_barrier
	ds_read2_b32 v[18:19], v38 offset0:0 offset1:32
	ds_read2_b32 v[20:21], v38 offset0:64 offset1:96
	ds_read2_b32 v[22:23], v38 offset0:128 offset1:160
	ds_read2_b32 v[24:25], v38 offset0:192 offset1:224
	ds_read2_b32 v[26:27], v87 offset0:0 offset1:32
	ds_read2_b32 v[28:29], v87 offset0:64 offset1:96
	ds_read2_b32 v[30:31], v87 offset0:128 offset1:160
	ds_read2_b32 v[32:33], v87 offset0:192 offset1:224
	s_waitcnt lgkmcnt(0)
	v_max3_f32 v48, v18, v19, v20
	v_max3_f32 v50, v21, v22, v23
	v_max3_f32 v48, v48, v24, v25
	v_max3_f32 v50, v50, v26, v27
	v_max3_f32 v48, v48, v28, v29
	v_max3_f32 v50, v50, v30, v31
	v_max3_f32 v48, v48, v32, v33
	v_max_f32_e32 v48, v48, v50
	v_mov_b32_e32 v50, v48
	s_nop 1
	v_permlane32_swap_b32_e32 v48, v50
	v_max_f32_e32 v48, v48, v50
	v_fmamk_f32 v48, v48, 0x3fb8aa3b, v34
	v_pk_fma_f32 v[18:19], v[18:19], v[84:85], v[48:49] op_sel_hi:[1,0,0] neg_lo:[0,0,1] neg_hi:[0,0,1]
	v_exp_f32_e32 v18, v18
	v_exp_f32_e32 v19, v19
	v_pk_fma_f32 v[20:21], v[20:21], v[84:85], v[48:49] op_sel_hi:[1,0,0] neg_lo:[0,0,1] neg_hi:[0,0,1]
	v_exp_f32_e32 v20, v20
	v_exp_f32_e32 v21, v21
	v_pk_fma_f32 v[22:23], v[22:23], v[84:85], v[48:49] op_sel_hi:[1,0,0] neg_lo:[0,0,1] neg_hi:[0,0,1]
	v_exp_f32_e32 v22, v22
	v_exp_f32_e32 v23, v23
	v_pk_fma_f32 v[24:25], v[24:25], v[84:85], v[48:49] op_sel_hi:[1,0,0] neg_lo:[0,0,1] neg_hi:[0,0,1]
	v_exp_f32_e32 v24, v24
	v_exp_f32_e32 v25, v25
	v_pk_fma_f32 v[26:27], v[26:27], v[84:85], v[48:49] op_sel_hi:[1,0,0] neg_lo:[0,0,1] neg_hi:[0,0,1]
	v_exp_f32_e32 v26, v26
	v_exp_f32_e32 v27, v27
	v_pk_fma_f32 v[28:29], v[28:29], v[84:85], v[48:49] op_sel_hi:[1,0,0] neg_lo:[0,0,1] neg_hi:[0,0,1]
	v_exp_f32_e32 v28, v28
	v_exp_f32_e32 v29, v29
	v_pk_fma_f32 v[30:31], v[30:31], v[84:85], v[48:49] op_sel_hi:[1,0,0] neg_lo:[0,0,1] neg_hi:[0,0,1]
	v_exp_f32_e32 v30, v30
	v_exp_f32_e32 v31, v31
	v_pk_fma_f32 v[32:33], v[32:33], v[84:85], v[48:49] op_sel_hi:[1,0,0] neg_lo:[0,0,1] neg_hi:[0,0,1]
	v_exp_f32_e32 v32, v32
	v_exp_f32_e32 v33, v33
	v_pk_add_f32 v[56:57], v[18:19], v[20:21]
	v_pk_add_f32 v[58:59], v[22:23], v[24:25]
	v_pk_add_f32 v[60:61], v[26:27], v[28:29]
	v_pk_add_f32 v[62:63], v[30:31], v[32:33]
	v_pk_add_f32 v[56:57], v[56:57], v[58:59]
	v_pk_add_f32 v[60:61], v[60:61], v[62:63]
	v_pk_add_f32 v[56:57], v[56:57], v[60:61]
	v_add_f32_e32 v50, v56, v57
	v_mov_b32_e32 v51, v50
	s_nop 1
	v_permlane32_swap_b32_e32 v50, v51
	v_add_f32_e32 v50, v50, v51
	v_log_f32_e32 v50, v50
	v_cvt_pk_f16_f32 v40, v18, v19
	v_cvt_pk_f16_f32 v41, v20, v21
	v_cvt_pk_f16_f32 v42, v22, v23
	v_cvt_pk_f16_f32 v43, v24, v25
	v_cvt_pk_f16_f32 v44, v26, v27
	v_cvt_pk_f16_f32 v45, v28, v29
	v_cvt_pk_f16_f32 v46, v30, v31
	v_cvt_pk_f16_f32 v47, v32, v33
	v_add_f32_e32 v50, 0x41600000, v50
	v_mul_f32_e32 v50, 0xbf317218, v50
	v_cndmask_b32_e64 v51, v50, 1.0, vcc
	s_waitcnt vmcnt(0)
	ds_read_b128 v[2:5], v39
	ds_read_b128 v[6:9], v81
	ds_read_b128 v[10:13], v82
	ds_read_b128 v[14:17], v83
	s_waitcnt lgkmcnt(2)
	v_max3_f32 v52, v2, v3, v4
	v_max3_f32 v53, v5, v6, v7
	v_max_f32_e32 v52, v52, v8
	v_max_f32_e32 v53, v53, v9
	s_waitcnt lgkmcnt(0)
	v_max3_f32 v52, v52, v10, v11
	v_max3_f32 v53, v53, v12, v13
	v_max3_f32 v52, v52, v14, v15
	v_max3_f32 v53, v53, v16, v17
	v_max_f32_e32 v52, v52, v53
	v_mov_b32_e32 v53, v52
	s_nop 1
	v_permlane32_swap_b32_e32 v52, v53
	v_max_f32_e32 v52, v52, v53
	v_cndmask_b32_e32 v54, 1.0, v52, vcc
	v_fmamk_f32 v48, v52, 0x3fb8aa3b, v34
	v_pk_fma_f32 v[2:3], v[2:3], v[84:85], v[48:49] op_sel_hi:[1,0,0] neg_lo:[0,0,1] neg_hi:[0,0,1]
	v_mfma_f32_32x32x2_f32 v[64:79], v54, v51, 0
	v_exp_f32_e32 v2, v2
	v_exp_f32_e32 v3, v3
	v_pk_fma_f32 v[4:5], v[4:5], v[84:85], v[48:49] op_sel_hi:[1,0,0] neg_lo:[0,0,1] neg_hi:[0,0,1]
	v_exp_f32_e32 v4, v4
	v_exp_f32_e32 v5, v5
	v_pk_fma_f32 v[6:7], v[6:7], v[84:85], v[48:49] op_sel_hi:[1,0,0] neg_lo:[0,0,1] neg_hi:[0,0,1]
	v_exp_f32_e32 v6, v6
	v_exp_f32_e32 v7, v7
	v_pk_fma_f32 v[8:9], v[8:9], v[84:85], v[48:49] op_sel_hi:[1,0,0] neg_lo:[0,0,1] neg_hi:[0,0,1]
	v_exp_f32_e32 v8, v8
	v_exp_f32_e32 v9, v9
	v_pk_fma_f32 v[10:11], v[10:11], v[84:85], v[48:49] op_sel_hi:[1,0,0] neg_lo:[0,0,1] neg_hi:[0,0,1]
	v_exp_f32_e32 v10, v10
	v_cvt_pk_f16_f32 v56, v2, v3
	v_cvt_pk_f16_f32 v57, v4, v5
	v_cvt_pk_f16_f32 v58, v6, v7
	v_cvt_pk_f16_f32 v59, v8, v9
	v_exp_f32_e32 v11, v11
	v_pk_fma_f32 v[12:13], v[12:13], v[84:85], v[48:49] op_sel_hi:[1,0,0] neg_lo:[0,0,1] neg_hi:[0,0,1]
	v_exp_f32_e32 v12, v12
	v_mfma_f32_32x32x16_f16 v[18:33], v[56:59], v[40:43], 0
	v_exp_f32_e32 v13, v13
	v_pk_fma_f32 v[14:15], v[14:15], v[84:85], v[48:49] op_sel_hi:[1,0,0] neg_lo:[0,0,1] neg_hi:[0,0,1]
	v_exp_f32_e32 v14, v14
	v_exp_f32_e32 v15, v15
	v_pk_fma_f32 v[16:17], v[16:17], v[84:85], v[48:49] op_sel_hi:[1,0,0] neg_lo:[0,0,1] neg_hi:[0,0,1]
	v_exp_f32_e32 v16, v16
	v_exp_f32_e32 v17, v17
	v_cvt_pk_f16_f32 v60, v10, v11
	v_cvt_pk_f16_f32 v61, v12, v13
	v_cvt_pk_f16_f32 v62, v14, v15
	v_cvt_pk_f16_f32 v63, v16, v17
	s_nop 1
	v_mfma_f32_32x32x16_f16 v[18:33], v[60:63], v[44:47], v[18:33]
	s_nop 11
	v_log_f32_e32 v18, v18
	v_log_f32_e32 v19, v19
	v_log_f32_e32 v20, v20
	v_log_f32_e32 v21, v21
	v_log_f32_e32 v22, v22
	v_log_f32_e32 v23, v23
	v_pk_fma_f32 v[64:65], v[18:19], v[84:85], v[64:65] op_sel:[0,1,0] op_sel_hi:[1,1,1]
	buffer_store_dword v64, v36, s[8:11], 0 offen
	buffer_store_dword v65, v36, s[8:11], s24 offen
	v_log_f32_e32 v24, v24
	v_log_f32_e32 v25, v25
	v_pk_fma_f32 v[66:67], v[20:21], v[84:85], v[66:67] op_sel:[0,1,0] op_sel_hi:[1,1,1]
	buffer_store_dword v66, v36, s[8:11], s25 offen
	buffer_store_dword v67, v36, s[8:11], s26 offen
	v_log_f32_e32 v26, v26
	v_log_f32_e32 v27, v27
	v_pk_fma_f32 v[68:69], v[22:23], v[84:85], v[68:69] op_sel:[0,1,0] op_sel_hi:[1,1,1]
	buffer_store_dword v68, v36, s[8:11], s27 offen
	buffer_store_dword v69, v36, s[8:11], s28 offen
	v_log_f32_e32 v28, v28
	v_log_f32_e32 v29, v29
	v_pk_fma_f32 v[70:71], v[24:25], v[84:85], v[70:71] op_sel:[0,1,0] op_sel_hi:[1,1,1]
	buffer_store_dword v70, v36, s[8:11], s29 offen
	buffer_store_dword v71, v36, s[8:11], s30 offen
	v_log_f32_e32 v30, v30
	v_log_f32_e32 v31, v31
	v_pk_fma_f32 v[72:73], v[26:27], v[84:85], v[72:73] op_sel:[0,1,0] op_sel_hi:[1,1,1]
	buffer_store_dword v72, v36, s[8:11], s31 offen
	buffer_store_dword v73, v36, s[8:11], s32 offen
	v_log_f32_e32 v32, v32
	v_log_f32_e32 v33, v33
	v_pk_fma_f32 v[74:75], v[28:29], v[84:85], v[74:75] op_sel:[0,1,0] op_sel_hi:[1,1,1]
	buffer_store_dword v74, v36, s[8:11], s33 offen
	buffer_store_dword v75, v36, s[8:11], s34 offen
	v_pk_fma_f32 v[76:77], v[30:31], v[84:85], v[76:77] op_sel:[0,1,0] op_sel_hi:[1,1,1]
	buffer_store_dword v76, v36, s[8:11], s35 offen
	buffer_store_dword v77, v36, s[8:11], s36 offen
	v_pk_fma_f32 v[78:79], v[32:33], v[84:85], v[78:79] op_sel:[0,1,0] op_sel_hi:[1,1,1]
	buffer_store_dword v78, v36, s[8:11], s37 offen
	buffer_store_dword v79, v36, s[8:11], s38 offen
	s_endpgm

	.amdhsa_kernel _Z16sum_layer_kernelPKfS0_Pf
		.amdhsa_group_segment_fixed_size 20480
		.amdhsa_private_segment_fixed_size 0
		.amdhsa_kernarg_size 24
		.amdhsa_user_sgpr_count 2
		.amdhsa_user_sgpr_dispatch_ptr 0
		.amdhsa_user_sgpr_queue_ptr 0
		.amdhsa_user_sgpr_kernarg_segment_ptr 1
		.amdhsa_user_sgpr_dispatch_id 0
		.amdhsa_user_sgpr_kernarg_preload_length 0
		.amdhsa_user_sgpr_kernarg_preload_offset 0
		.amdhsa_user_sgpr_private_segment_size 0
		.amdhsa_uses_dynamic_stack 0
		.amdhsa_enable_private_segment 0
		.amdhsa_system_sgpr_workgroup_id_x 1
		.amdhsa_system_sgpr_workgroup_id_y 0
		.amdhsa_system_sgpr_workgroup_id_z 0
		.amdhsa_system_sgpr_workgroup_info 0
		.amdhsa_system_vgpr_workitem_id 0
		.amdhsa_next_free_vgpr 88
		.amdhsa_next_free_sgpr 56
		.amdhsa_accum_offset 88
		.amdhsa_reserve_vcc 1
		.amdhsa_float_round_mode_32 0
		.amdhsa_float_round_mode_16_64 0
		.amdhsa_float_denorm_mode_32 3
		.amdhsa_float_denorm_mode_16_64 3
		.amdhsa_dx10_clamp 1
		.amdhsa_ieee_mode 1
		.amdhsa_fp16_overflow 0
		.amdhsa_tg_split 0
		.amdhsa_exception_fp_ieee_invalid_op 0
		.amdhsa_exception_fp_denorm_src 0
		.amdhsa_exception_fp_ieee_div_zero 0
		.amdhsa_exception_fp_ieee_overflow 0
		.amdhsa_exception_fp_ieee_underflow 0
		.amdhsa_exception_fp_ieee_inexact 0
		.amdhsa_exception_int_div_zero 0
	.end_amdhsa_kernel

amdhsa.kernels:
  - .agpr_count:     0
    .args:
      - .address_space:  global
        .offset:         0
        .size:           8
        .value_kind:     global_buffer
      - .address_space:  global
        .offset:         8
        .size:           8
        .value_kind:     global_buffer
      - .address_space:  global
        .offset:         16
        .size:           8
        .value_kind:     global_buffer
    .group_segment_fixed_size: 20480
    .kernarg_segment_align: 8
    .kernarg_segment_size: 24
    .language:       OpenCL C
    .language_version:
      - 2
      - 0
    .max_flat_workgroup_size: 256
    .name:           _Z16sum_layer_kernelPKfS0_Pf
    .private_segment_fixed_size: 0
    .sgpr_count:     62
    .sgpr_spill_count: 0
    .symbol:         _Z16sum_layer_kernelPKfS0_Pf.kd
    .uniform_work_group_size: 1
    .uses_dynamic_stack: false
    .vgpr_count:     88
    .vgpr_spill_count: 0
    .wavefront_size: 64
